# yp stored in blocked [slot/128][D/128][128][128] layout (P8 stores to consecutive lines, P9 reads whole lines)
# baseline (speedup 1.0000x reference)
.LBB0_1047:
	s_ashr_i32 s7, s6, 31
	s_lshl_b64 s[26:27], s[6:7], 13
	s_add_u32 s7, s86, s26
	s_addc_u32 s28, s87, s27
	s_ashr_i32 s11, s10, 31
	s_lshl_b64 s[26:27], s[10:11], 2
	s_add_u32 s7, s7, s26
	s_addc_u32 s27, s28, s27
	s_add_u32 s26, s7, s72
	s_addc_u32 s27, s27, 0
	global_load_dwordx4 v[12:15], v198, s[26:27]
	global_load_dwordx4 v[8:11], v198, s[26:27] offset:64
	global_load_dwordx4 v[4:7], v198, s[26:27] offset:512
	global_load_dwordx4 v[0:3], v198, s[26:27] offset:576
	s_andn2_b64 vcc, exec, s[24:25]
	s_lshr_b32 s28, s44, 7
	s_lshl_b32 s28, s28, 18
	s_lshr_b32 s29, s10, 7
	s_lshl_b32 s29, s29, 14
	s_add_u32 s28, s28, s29
	s_add_u32 s28, s28, s14
	s_add_u32 s100, s16, s28
	s_addc_u32 s101, s17, 0
	v_bfe_u32 v251, v178, 4, 2
	v_lshl_add_u32 v16, v251, 4, v193
	v_lshlrev_b32_e32 v16, 7, v16
	v_mov_b32_e32 v17, 0
	v_lshl_add_u64 v[252:253], s[100:101], 0, v[16:17]
	s_mov_b64 s[100:101], 0x4000
	v_lshl_add_u64 v[254:255], v[252:253], 0, s[100:101]
	s_mov_b64 s[100:101], 0x40000
	v_lshl_add_u64 v[226:227], v[252:253], 0, s[100:101]
	v_lshl_add_u64 v[228:229], v[254:255], 0, s[100:101]
	s_waitcnt vmcnt(0)
	v_pk_add_f32 v[24:25], v[172:173], v[12:13]
	v_pk_add_f32 v[26:27], v[174:175], v[14:15]
	v_pk_add_f32 v[28:29], v[164:165], v[12:13]
	v_pk_add_f32 v[30:31], v[166:167], v[14:15]
	v_pk_add_f32 v[32:33], v[156:157], v[12:13]
	v_pk_add_f32 v[34:35], v[158:159], v[14:15]
	v_pk_add_f32 v[36:37], v[148:149], v[12:13]
	v_pk_add_f32 v[38:39], v[150:151], v[14:15]
	v_med3_f32 v24, v24, s77, v200
	v_med3_f32 v25, v25, s77, v200
	v_med3_f32 v26, v26, s77, v200
	v_med3_f32 v27, v27, s77, v200
	v_med3_f32 v28, v28, s77, v200
	v_med3_f32 v29, v29, s77, v200
	v_med3_f32 v30, v30, s77, v200
	v_med3_f32 v31, v31, s77, v200
	v_med3_f32 v32, v32, s77, v200
	v_med3_f32 v33, v33, s77, v200
	v_med3_f32 v34, v34, s77, v200
	v_med3_f32 v35, v35, s77, v200
	v_med3_f32 v36, v36, s77, v200
	v_med3_f32 v37, v37, s77, v200
	v_med3_f32 v38, v38, s77, v200
	v_med3_f32 v39, v39, s77, v200
	v_cvt_pk_fp8_f32 v20, v24, v25
	v_cvt_pk_fp8_f32 v21, v28, v29
	v_cvt_pk_fp8_f32 v22, v32, v33
	v_cvt_pk_fp8_f32 v23, v36, v37
	v_cvt_pk_fp8_f32 v20, v26, v27 op_sel:[0,0,1]
	v_cvt_pk_fp8_f32 v21, v30, v31 op_sel:[0,0,1]
	v_cvt_pk_fp8_f32 v22, v34, v35 op_sel:[0,0,1]
	v_cvt_pk_fp8_f32 v23, v38, v39 op_sel:[0,0,1]
	s_nop 1
	v_permlane32_swap_b32_e32 v20, v22
	v_permlane32_swap_b32_e32 v21, v23
	s_nop 1
	v_permlane16_swap_b32_e32 v20, v21
	v_permlane16_swap_b32_e32 v22, v23
	global_store_dwordx4 v[252:253], v[20:23], off
	v_pk_add_f32 v[24:25], v[168:169], v[8:9]
	v_pk_add_f32 v[26:27], v[170:171], v[10:11]
	v_pk_add_f32 v[28:29], v[160:161], v[8:9]
	v_pk_add_f32 v[30:31], v[162:163], v[10:11]
	v_pk_add_f32 v[32:33], v[152:153], v[8:9]
	v_pk_add_f32 v[34:35], v[154:155], v[10:11]
	v_pk_add_f32 v[36:37], v[144:145], v[8:9]
	v_pk_add_f32 v[38:39], v[146:147], v[10:11]
	v_med3_f32 v24, v24, s77, v200
	v_med3_f32 v25, v25, s77, v200
	v_med3_f32 v26, v26, s77, v200
	v_med3_f32 v27, v27, s77, v200
	v_med3_f32 v28, v28, s77, v200
	v_med3_f32 v29, v29, s77, v200
	v_med3_f32 v30, v30, s77, v200
	v_med3_f32 v31, v31, s77, v200
	v_med3_f32 v32, v32, s77, v200
	v_med3_f32 v33, v33, s77, v200
	v_med3_f32 v34, v34, s77, v200
	v_med3_f32 v35, v35, s77, v200
	v_med3_f32 v36, v36, s77, v200
	v_med3_f32 v37, v37, s77, v200
	v_med3_f32 v38, v38, s77, v200
	v_med3_f32 v39, v39, s77, v200
	v_cvt_pk_fp8_f32 v40, v24, v25
	v_cvt_pk_fp8_f32 v41, v28, v29
	v_cvt_pk_fp8_f32 v42, v32, v33
	v_cvt_pk_fp8_f32 v43, v36, v37
	v_cvt_pk_fp8_f32 v40, v26, v27 op_sel:[0,0,1]
	v_cvt_pk_fp8_f32 v41, v30, v31 op_sel:[0,0,1]
	v_cvt_pk_fp8_f32 v42, v34, v35 op_sel:[0,0,1]
	v_cvt_pk_fp8_f32 v43, v38, v39 op_sel:[0,0,1]
	s_nop 1
	v_permlane32_swap_b32_e32 v40, v42
	v_permlane32_swap_b32_e32 v41, v43
	s_nop 1
	v_permlane16_swap_b32_e32 v40, v41
	v_permlane16_swap_b32_e32 v42, v43
	global_store_dwordx4 v[252:253], v[40:43], off offset:16
	v_pk_add_f32 v[24:25], v[140:141], v[4:5]
	v_pk_add_f32 v[26:27], v[142:143], v[6:7]
	v_pk_add_f32 v[28:29], v[132:133], v[4:5]
	v_pk_add_f32 v[30:31], v[134:135], v[6:7]
	v_pk_add_f32 v[32:33], v[124:125], v[4:5]
	v_pk_add_f32 v[34:35], v[126:127], v[6:7]
	v_pk_add_f32 v[36:37], v[116:117], v[4:5]
	v_pk_add_f32 v[38:39], v[118:119], v[6:7]
	v_med3_f32 v24, v24, s77, v200
	v_med3_f32 v25, v25, s77, v200
	v_med3_f32 v26, v26, s77, v200
	v_med3_f32 v27, v27, s77, v200
	v_med3_f32 v28, v28, s77, v200
	v_med3_f32 v29, v29, s77, v200
	v_med3_f32 v30, v30, s77, v200
	v_med3_f32 v31, v31, s77, v200
	v_med3_f32 v32, v32, s77, v200
	v_med3_f32 v33, v33, s77, v200
	v_med3_f32 v34, v34, s77, v200
	v_med3_f32 v35, v35, s77, v200
	v_med3_f32 v36, v36, s77, v200
	v_med3_f32 v37, v37, s77, v200
	v_med3_f32 v38, v38, s77, v200
	v_med3_f32 v39, v39, s77, v200
	v_cvt_pk_fp8_f32 v20, v24, v25
	v_cvt_pk_fp8_f32 v21, v28, v29
	v_cvt_pk_fp8_f32 v22, v32, v33
	v_cvt_pk_fp8_f32 v23, v36, v37
	v_cvt_pk_fp8_f32 v20, v26, v27 op_sel:[0,0,1]
	v_cvt_pk_fp8_f32 v21, v30, v31 op_sel:[0,0,1]
	v_cvt_pk_fp8_f32 v22, v34, v35 op_sel:[0,0,1]
	v_cvt_pk_fp8_f32 v23, v38, v39 op_sel:[0,0,1]
	s_nop 1
	v_permlane32_swap_b32_e32 v20, v22
	v_permlane32_swap_b32_e32 v21, v23
	s_nop 1
	v_permlane16_swap_b32_e32 v20, v21
	v_permlane16_swap_b32_e32 v22, v23
	global_store_dwordx4 v[254:255], v[20:23], off
	v_pk_add_f32 v[24:25], v[136:137], v[0:1]
	v_pk_add_f32 v[26:27], v[138:139], v[2:3]
	v_pk_add_f32 v[28:29], v[128:129], v[0:1]
	v_pk_add_f32 v[30:31], v[130:131], v[2:3]
	v_pk_add_f32 v[32:33], v[120:121], v[0:1]
	v_pk_add_f32 v[34:35], v[122:123], v[2:3]
	v_pk_add_f32 v[36:37], v[112:113], v[0:1]
	v_pk_add_f32 v[38:39], v[114:115], v[2:3]
	v_med3_f32 v24, v24, s77, v200
	v_med3_f32 v25, v25, s77, v200
	v_med3_f32 v26, v26, s77, v200
	v_med3_f32 v27, v27, s77, v200
	v_med3_f32 v28, v28, s77, v200
	v_med3_f32 v29, v29, s77, v200
	v_med3_f32 v30, v30, s77, v200
	v_med3_f32 v31, v31, s77, v200
	v_med3_f32 v32, v32, s77, v200
	v_med3_f32 v33, v33, s77, v200
	v_med3_f32 v34, v34, s77, v200
	v_med3_f32 v35, v35, s77, v200
	v_med3_f32 v36, v36, s77, v200
	v_med3_f32 v37, v37, s77, v200
	v_med3_f32 v38, v38, s77, v200
	v_med3_f32 v39, v39, s77, v200
	v_cvt_pk_fp8_f32 v40, v24, v25
	v_cvt_pk_fp8_f32 v41, v28, v29
	v_cvt_pk_fp8_f32 v42, v32, v33
	v_cvt_pk_fp8_f32 v43, v36, v37
	v_cvt_pk_fp8_f32 v40, v26, v27 op_sel:[0,0,1]
	v_cvt_pk_fp8_f32 v41, v30, v31 op_sel:[0,0,1]
	v_cvt_pk_fp8_f32 v42, v34, v35 op_sel:[0,0,1]
	v_cvt_pk_fp8_f32 v43, v38, v39 op_sel:[0,0,1]
	s_nop 1
	v_permlane32_swap_b32_e32 v40, v42
	v_permlane32_swap_b32_e32 v41, v43
	s_nop 1
	v_permlane16_swap_b32_e32 v40, v41
	v_permlane16_swap_b32_e32 v42, v43
	global_store_dwordx4 v[254:255], v[40:43], off offset:16
	v_pk_add_f32 v[24:25], v[108:109], v[12:13]
	v_pk_add_f32 v[26:27], v[110:111], v[14:15]
	v_pk_add_f32 v[28:29], v[100:101], v[12:13]
	v_pk_add_f32 v[30:31], v[102:103], v[14:15]
	v_pk_add_f32 v[32:33], v[92:93], v[12:13]
	v_pk_add_f32 v[34:35], v[94:95], v[14:15]
	v_pk_add_f32 v[36:37], v[84:85], v[12:13]
	v_pk_add_f32 v[38:39], v[86:87], v[14:15]
	v_med3_f32 v24, v24, s77, v200
	v_med3_f32 v25, v25, s77, v200
	v_med3_f32 v26, v26, s77, v200
	v_med3_f32 v27, v27, s77, v200
	v_med3_f32 v28, v28, s77, v200
	v_med3_f32 v29, v29, s77, v200
	v_med3_f32 v30, v30, s77, v200
	v_med3_f32 v31, v31, s77, v200
	v_med3_f32 v32, v32, s77, v200
	v_med3_f32 v33, v33, s77, v200
	v_med3_f32 v34, v34, s77, v200
	v_med3_f32 v35, v35, s77, v200
	v_med3_f32 v36, v36, s77, v200
	v_med3_f32 v37, v37, s77, v200
	v_med3_f32 v38, v38, s77, v200
	v_med3_f32 v39, v39, s77, v200
	v_cvt_pk_fp8_f32 v20, v24, v25
	v_cvt_pk_fp8_f32 v21, v28, v29
	v_cvt_pk_fp8_f32 v22, v32, v33
	v_cvt_pk_fp8_f32 v23, v36, v37
	v_cvt_pk_fp8_f32 v20, v26, v27 op_sel:[0,0,1]
	v_cvt_pk_fp8_f32 v21, v30, v31 op_sel:[0,0,1]
	v_cvt_pk_fp8_f32 v22, v34, v35 op_sel:[0,0,1]
	v_cvt_pk_fp8_f32 v23, v38, v39 op_sel:[0,0,1]
	s_nop 1
	v_permlane32_swap_b32_e32 v20, v22
	v_permlane32_swap_b32_e32 v21, v23
	s_nop 1
	v_permlane16_swap_b32_e32 v20, v21
	v_permlane16_swap_b32_e32 v22, v23
	global_store_dwordx4 v[226:227], v[20:23], off
	v_pk_add_f32 v[24:25], v[104:105], v[8:9]
	v_pk_add_f32 v[26:27], v[106:107], v[10:11]
	v_pk_add_f32 v[28:29], v[96:97], v[8:9]
	v_pk_add_f32 v[30:31], v[98:99], v[10:11]
	v_pk_add_f32 v[32:33], v[88:89], v[8:9]
	v_pk_add_f32 v[34:35], v[90:91], v[10:11]
	v_pk_add_f32 v[36:37], v[80:81], v[8:9]
	v_pk_add_f32 v[38:39], v[82:83], v[10:11]
	v_med3_f32 v24, v24, s77, v200
	v_med3_f32 v25, v25, s77, v200
	v_med3_f32 v26, v26, s77, v200
	v_med3_f32 v27, v27, s77, v200
	v_med3_f32 v28, v28, s77, v200
	v_med3_f32 v29, v29, s77, v200
	v_med3_f32 v30, v30, s77, v200
	v_med3_f32 v31, v31, s77, v200
	v_med3_f32 v32, v32, s77, v200
	v_med3_f32 v33, v33, s77, v200
	v_med3_f32 v34, v34, s77, v200
	v_med3_f32 v35, v35, s77, v200
	v_med3_f32 v36, v36, s77, v200
	v_med3_f32 v37, v37, s77, v200
	v_med3_f32 v38, v38, s77, v200
	v_med3_f32 v39, v39, s77, v200
	v_cvt_pk_fp8_f32 v40, v24, v25
	v_cvt_pk_fp8_f32 v41, v28, v29
	v_cvt_pk_fp8_f32 v42, v32, v33
	v_cvt_pk_fp8_f32 v43, v36, v37
	v_cvt_pk_fp8_f32 v40, v26, v27 op_sel:[0,0,1]
	v_cvt_pk_fp8_f32 v41, v30, v31 op_sel:[0,0,1]
	v_cvt_pk_fp8_f32 v42, v34, v35 op_sel:[0,0,1]
	v_cvt_pk_fp8_f32 v43, v38, v39 op_sel:[0,0,1]
	s_nop 1
	v_permlane32_swap_b32_e32 v40, v42
	v_permlane32_swap_b32_e32 v41, v43
	s_nop 1
	v_permlane16_swap_b32_e32 v40, v41
	v_permlane16_swap_b32_e32 v42, v43
	global_store_dwordx4 v[226:227], v[40:43], off offset:16
	v_pk_add_f32 v[24:25], v[76:77], v[4:5]
	v_pk_add_f32 v[26:27], v[78:79], v[6:7]
	v_pk_add_f32 v[28:29], v[68:69], v[4:5]
	v_pk_add_f32 v[30:31], v[70:71], v[6:7]
	v_pk_add_f32 v[32:33], v[60:61], v[4:5]
	v_pk_add_f32 v[34:35], v[62:63], v[6:7]
	v_pk_add_f32 v[36:37], v[52:53], v[4:5]
	v_pk_add_f32 v[38:39], v[54:55], v[6:7]
	v_med3_f32 v24, v24, s77, v200
	v_med3_f32 v25, v25, s77, v200
	v_med3_f32 v26, v26, s77, v200
	v_med3_f32 v27, v27, s77, v200
	v_med3_f32 v28, v28, s77, v200
	v_med3_f32 v29, v29, s77, v200
	v_med3_f32 v30, v30, s77, v200
	v_med3_f32 v31, v31, s77, v200
	v_med3_f32 v32, v32, s77, v200
	v_med3_f32 v33, v33, s77, v200
	v_med3_f32 v34, v34, s77, v200
	v_med3_f32 v35, v35, s77, v200
	v_med3_f32 v36, v36, s77, v200
	v_med3_f32 v37, v37, s77, v200
	v_med3_f32 v38, v38, s77, v200
	v_med3_f32 v39, v39, s77, v200
	v_cvt_pk_fp8_f32 v20, v24, v25
	v_cvt_pk_fp8_f32 v21, v28, v29
	v_cvt_pk_fp8_f32 v22, v32, v33
	v_cvt_pk_fp8_f32 v23, v36, v37
	v_cvt_pk_fp8_f32 v20, v26, v27 op_sel:[0,0,1]
	v_cvt_pk_fp8_f32 v21, v30, v31 op_sel:[0,0,1]
	v_cvt_pk_fp8_f32 v22, v34, v35 op_sel:[0,0,1]
	v_cvt_pk_fp8_f32 v23, v38, v39 op_sel:[0,0,1]
	s_nop 1
	v_permlane32_swap_b32_e32 v20, v22
	v_permlane32_swap_b32_e32 v21, v23
	s_nop 1
	v_permlane16_swap_b32_e32 v20, v21
	v_permlane16_swap_b32_e32 v22, v23
	global_store_dwordx4 v[228:229], v[20:23], off
	v_pk_add_f32 v[24:25], v[72:73], v[0:1]
	v_pk_add_f32 v[26:27], v[74:75], v[2:3]
	v_pk_add_f32 v[28:29], v[64:65], v[0:1]
	v_pk_add_f32 v[30:31], v[66:67], v[2:3]
	v_pk_add_f32 v[32:33], v[56:57], v[0:1]
	v_pk_add_f32 v[34:35], v[58:59], v[2:3]
	v_pk_add_f32 v[36:37], v[48:49], v[0:1]
	v_pk_add_f32 v[38:39], v[50:51], v[2:3]
	v_med3_f32 v24, v24, s77, v200
	v_med3_f32 v25, v25, s77, v200
	v_med3_f32 v26, v26, s77, v200
	v_med3_f32 v27, v27, s77, v200
	v_med3_f32 v28, v28, s77, v200
	v_med3_f32 v29, v29, s77, v200
	v_med3_f32 v30, v30, s77, v200
	v_med3_f32 v31, v31, s77, v200
	v_med3_f32 v32, v32, s77, v200
	v_med3_f32 v33, v33, s77, v200
	v_med3_f32 v34, v34, s77, v200
	v_med3_f32 v35, v35, s77, v200
	v_med3_f32 v36, v36, s77, v200
	v_med3_f32 v37, v37, s77, v200
	v_med3_f32 v38, v38, s77, v200
	v_med3_f32 v39, v39, s77, v200
	v_cvt_pk_fp8_f32 v40, v24, v25
	v_cvt_pk_fp8_f32 v41, v28, v29
	v_cvt_pk_fp8_f32 v42, v32, v33
	v_cvt_pk_fp8_f32 v43, v36, v37
	v_cvt_pk_fp8_f32 v40, v26, v27 op_sel:[0,0,1]
	v_cvt_pk_fp8_f32 v41, v30, v31 op_sel:[0,0,1]
	v_cvt_pk_fp8_f32 v42, v34, v35 op_sel:[0,0,1]
	v_cvt_pk_fp8_f32 v43, v38, v39 op_sel:[0,0,1]
	s_nop 1
	v_permlane32_swap_b32_e32 v40, v42
	v_permlane32_swap_b32_e32 v41, v43
	s_nop 1
	v_permlane16_swap_b32_e32 v40, v41
	v_permlane16_swap_b32_e32 v42, v43
	global_store_dwordx4 v[228:229], v[40:43], off offset:16
	s_cbranch_vccnz .LBB0_994
	v_mov_b32_e32 v48, 0
	s_mov_b32 s81, s79
	s_mov_b64 s[8:9], s[22:23]
	s_mov_b32 s6, s20
	s_mov_b32 s44, s82
	s_mov_b32 s10, s21
	s_mov_b32 s80, s71
	v_mov_b32_e32 v49, v48
	v_mov_b32_e32 v50, v48
	v_mov_b32_e32 v51, v48
	v_mov_b32_e32 v52, v48
	v_mov_b32_e32 v53, v48
	v_mov_b32_e32 v54, v48
	v_mov_b32_e32 v55, v48
	v_mov_b32_e32 v56, v48
	v_mov_b32_e32 v57, v48
	v_mov_b32_e32 v58, v48
	v_mov_b32_e32 v59, v48
	v_mov_b32_e32 v60, v48
	v_mov_b32_e32 v61, v48
	v_mov_b32_e32 v62, v48
	v_mov_b32_e32 v63, v48
	v_mov_b32_e32 v64, v48
	v_mov_b32_e32 v65, v48
	v_mov_b32_e32 v66, v48
	v_mov_b32_e32 v67, v48
	v_mov_b32_e32 v68, v48
	v_mov_b32_e32 v69, v48
	v_mov_b32_e32 v70, v48
	v_mov_b32_e32 v71, v48
	v_mov_b32_e32 v72, v48
	v_mov_b32_e32 v73, v48
	v_mov_b32_e32 v74, v48
	v_mov_b32_e32 v75, v48
	v_mov_b32_e32 v76, v48
	v_mov_b32_e32 v77, v48
	v_mov_b32_e32 v78, v48
	v_mov_b32_e32 v79, v48
	v_mov_b32_e32 v80, v48
	v_mov_b32_e32 v81, v48
	v_mov_b32_e32 v82, v48
	v_mov_b32_e32 v83, v48
	v_mov_b32_e32 v84, v48
	v_mov_b32_e32 v85, v48
	v_mov_b32_e32 v86, v48
	v_mov_b32_e32 v87, v48
	v_mov_b32_e32 v88, v48
	v_mov_b32_e32 v89, v48
	v_mov_b32_e32 v90, v48
	v_mov_b32_e32 v91, v48
	v_mov_b32_e32 v92, v48
	v_mov_b32_e32 v93, v48
	v_mov_b32_e32 v94, v48
	v_mov_b32_e32 v95, v48
	v_mov_b32_e32 v96, v48
	v_mov_b32_e32 v97, v48
	v_mov_b32_e32 v98, v48
	v_mov_b32_e32 v99, v48
	v_mov_b32_e32 v100, v48
	v_mov_b32_e32 v101, v48
	v_mov_b32_e32 v102, v48
	v_mov_b32_e32 v103, v48
	v_mov_b32_e32 v104, v48
	v_mov_b32_e32 v105, v48
	v_mov_b32_e32 v106, v48
	v_mov_b32_e32 v107, v48
	v_mov_b32_e32 v108, v48
	v_mov_b32_e32 v109, v48
	v_mov_b32_e32 v110, v48
	v_mov_b32_e32 v111, v48
	v_mov_b32_e32 v112, v48
	v_mov_b32_e32 v113, v48
	v_mov_b32_e32 v114, v48
	v_mov_b32_e32 v115, v48
	v_mov_b32_e32 v116, v48
	v_mov_b32_e32 v117, v48
	v_mov_b32_e32 v118, v48
	v_mov_b32_e32 v119, v48
	v_mov_b32_e32 v120, v48
	v_mov_b32_e32 v121, v48
	v_mov_b32_e32 v122, v48
	v_mov_b32_e32 v123, v48
	v_mov_b32_e32 v124, v48
	v_mov_b32_e32 v125, v48
	v_mov_b32_e32 v126, v48
	v_mov_b32_e32 v127, v48
	v_mov_b32_e32 v128, v48
	v_mov_b32_e32 v129, v48
	v_mov_b32_e32 v130, v48
	v_mov_b32_e32 v131, v48
	v_mov_b32_e32 v132, v48
	v_mov_b32_e32 v133, v48
	v_mov_b32_e32 v134, v48
	v_mov_b32_e32 v135, v48
	v_mov_b32_e32 v136, v48
	v_mov_b32_e32 v137, v48
	v_mov_b32_e32 v138, v48
	v_mov_b32_e32 v139, v48
	v_mov_b32_e32 v140, v48
	v_mov_b32_e32 v141, v48
	v_mov_b32_e32 v142, v48
	v_mov_b32_e32 v143, v48
	v_mov_b32_e32 v144, v48
	v_mov_b32_e32 v145, v48
	v_mov_b32_e32 v146, v48
	v_mov_b32_e32 v147, v48
	v_mov_b32_e32 v148, v48
	v_mov_b32_e32 v149, v48
	v_mov_b32_e32 v150, v48
	v_mov_b32_e32 v151, v48
	v_mov_b32_e32 v152, v48
	v_mov_b32_e32 v153, v48
	v_mov_b32_e32 v154, v48
	v_mov_b32_e32 v155, v48
	v_mov_b32_e32 v156, v48
	v_mov_b32_e32 v157, v48
	v_mov_b32_e32 v158, v48
	v_mov_b32_e32 v159, v48
	v_mov_b32_e32 v160, v48
	v_mov_b32_e32 v161, v48
	v_mov_b32_e32 v162, v48
	v_mov_b32_e32 v163, v48
	v_mov_b32_e32 v164, v48
	v_mov_b32_e32 v165, v48
	v_mov_b32_e32 v166, v48
	v_mov_b32_e32 v167, v48
	v_mov_b32_e32 v168, v48
	v_mov_b32_e32 v169, v48
	v_mov_b32_e32 v170, v48
	v_mov_b32_e32 v171, v48
	v_mov_b32_e32 v172, v48
	v_mov_b32_e32 v173, v48
	v_mov_b32_e32 v174, v48
	v_mov_b32_e32 v175, v48
	s_branch .LBB0_994

.LBB0_1092:
	s_or_b64 exec, exec, s[0:1]
	s_waitcnt vmcnt(0)
	v_lshl_add_u32 v12, s33, 3, v179
	s_movk_i32 s0, 0x2000
	v_cmp_gt_i32_e32 vcc, s0, v12
	s_waitcnt lgkmcnt(0)
	s_barrier
	s_and_saveexec_b64 s[0:1], vcc
	s_cbranch_execz .LBB0_1095
	v_lshlrev_b32_e32 v0, 3, v178
	v_and_b32_e32 v14, 0x1f8, v0
	v_mov_b32_e32 v15, 0
	v_lshl_add_u64 v[0:1], s[90:91], 0, v[14:15]
	s_mov_b64 s[6:7], 0x191a0000
	v_ashrrev_i32_e32 v13, 31, v12
	s_add_u32 s0, s90, 0xf040000
	v_lshl_add_u64 v[16:17], v[0:1], 0, s[6:7]
	v_bfe_u32 v104, v178, 4, 2
	v_mov_b32_e32 v105, 0
	v_mul_u32_u24_e32 v104, 0x3f80, v104
	v_lshl_add_u64 v[16:17], v[16:17], 0, v[104:105]
	s_mov_b64 s[24:25], 0x10000
	s_mov_b64 s[26:27], 0x20000
	s_mov_b64 s[28:29], 0x30000
	v_lshlrev_b64 v[0:1], 12, v[12:13]
	v_and_b32_e32 v2, 63, v178
	s_addc_u32 s1, s91, 0
	v_lshl_or_b32 v0, v2, 4, v0
	s_add_u32 s2, s90, 0xf060000
	v_lshl_add_u64 v[0:1], s[90:91], 0, v[0:1]
	s_mov_b64 s[8:9], 0x9040000
	s_addc_u32 s3, s91, 0
	v_lshl_add_u64 v[18:19], v[0:1], 0, s[8:9]
	v_lshlrev_b32_e32 v0, 2, v179
	s_add_u32 s4, s90, 0xf080000
	v_lshl_add_u32 v20, s33, 5, v0
	v_lshlrev_b64 v[0:1], 13, v[12:13]
	s_addc_u32 s5, s91, 0
	s_lshl_b32 s6, s96, 3
	v_lshl_or_b32 v0, v2, 5, v0
	s_ashr_i32 s7, s6, 31
	v_lshl_add_u64 v[0:1], s[88:89], 0, v[0:1]
	s_mov_b64 s[10:11], 0x1000
	s_lshl_b64 s[8:9], s[6:7], 12
	v_lshl_add_u64 v[22:23], v[0:1], 0, s[10:11]
	s_lshl_b64 s[10:11], s[6:7], 13
	s_mov_b32 s7, 0x20840
	s_lshl_b32 s20, s96, 5
	s_mov_b64 s[12:13], 0
	s_addk_i32 s7, 0x100
	v_lshlrev_b32_e32 v14, 2, v14
	s_mov_b64 s[14:15], 0xa000
	s_mov_b64 s[16:17], 0xb000
	s_mov_b32 s21, 0xb000
	s_mov_b64 s[18:19], 0xb800
	s_movk_i32 s22, 0x1fff
.LBB0_1094:
	v_ashrrev_i32_e32 v21, 31, v20
	v_add_u32_e32 v0, 1, v20
	v_add_u32_e32 v2, 2, v20
	v_lshlrev_b64 v[4:5], 2, v[20:21]
	v_ashrrev_i32_e32 v1, 31, v0
	v_ashrrev_i32_e32 v3, 31, v2
	v_lshl_add_u64 v[6:7], s[0:1], 0, v[4:5]
	v_lshl_add_u64 v[8:9], s[2:3], 0, v[4:5]
	v_lshl_add_u64 v[4:5], s[4:5], 0, v[4:5]
	v_lshlrev_b64 v[10:11], 2, v[0:1]
	v_lshl_add_u64 v[24:25], v[2:3], 2, s[4:5]
	global_load_dwordx4 v[0:3], v[6:7], off
	global_load_dword v13, v[8:9], off
	global_load_dword v21, v[4:5], off
	v_lshl_add_u64 v[4:5], s[2:3], 0, v[10:11]
	v_lshl_add_u64 v[6:7], s[4:5], 0, v[10:11]
	global_load_dwordx3 v[8:10], v[4:5], off
	global_load_dword v11, v[6:7], off
	global_load_dwordx2 v[26:27], v[24:25], off
	v_ashrrev_i32_e32 v4, 31, v12
	v_lshrrev_b32_e32 v4, 21, v4
	v_add_u32_e32 v4, v12, v4
	v_ashrrev_i32_e32 v4, 11, v4
	v_mul_i32_i24_e32 v4, 0x3000, v4
	v_ashrrev_i32_e32 v5, 31, v4
	v_lshl_add_u64 v[4:5], v[4:5], 2, s[92:93]
	v_lshl_add_u64 v[28:29], v[4:5], 0, v[14:15]
	v_add_co_u32_e32 v24, vcc, s21, v28
	global_load_dwordx4 v[36:39], v[18:19], off
	s_nop 0
	v_addc_co_u32_e32 v25, vcc, 0, v29, vcc
	global_load_dwordx4 v[4:7], v[24:25], off offset:-4096
	v_lshl_add_u64 v[30:31], v[28:29], 0, s[14:15]
	v_add_u32_e32 v12, s6, v12
	v_cmp_lt_i32_e32 vcc, s22, v12
	v_add_u32_e32 v20, s20, v20
	s_or_b64 s[12:13], vcc, s[12:13]
	s_waitcnt vmcnt(6)
	v_lshl_add_u32 v13, v13, 2, s7
	ds_read_b32 v13, v13 offset:128
	s_waitcnt vmcnt(4)
	v_lshl_add_u32 v8, v8, 2, s7
	v_lshl_add_u32 v9, v9, 2, s7
	v_lshl_add_u32 v10, v10, 2, s7
	ds_read_b32 v32, v8 offset:128
	ds_read_b32 v33, v9 offset:128
	ds_read_b32 v34, v10 offset:128
	s_waitcnt lgkmcnt(3)
	v_add_u32_e32 v8, v21, v13
	v_ashrrev_i32_e32 v9, 31, v8
	v_and_b32_e32 v9, 0x7f, v8
	v_lshrrev_b32_e32 v8, 7, v8
	v_lshlrev_b32_e32 v9, 7, v9
	v_lshl_or_b32 v8, v8, 18, v9
	v_mov_b32_e32 v9, 0
	v_lshl_add_u64 v[44:45], v[16:17], 0, v[8:9]
	global_load_dwordx2 v[46:47], v[44:45], off
	s_waitcnt vmcnt(4) lgkmcnt(2)
	v_add_u32_e32 v10, v11, v32
	s_waitcnt vmcnt(3) lgkmcnt(1)
	v_add_u32_e32 v26, v26, v33
	s_waitcnt lgkmcnt(0)
	v_add_u32_e32 v32, v27, v34
	v_ashrrev_i32_e32 v11, 31, v10
	v_ashrrev_i32_e32 v27, 31, v26
	v_ashrrev_i32_e32 v33, 31, v32
	v_and_b32_e32 v9, 0x7f, v10
	v_lshrrev_b32_e32 v8, 7, v10
	v_lshlrev_b32_e32 v9, 7, v9
	v_lshl_or_b32 v8, v8, 18, v9
	v_mov_b32_e32 v9, 0
	v_and_b32_e32 v11, 0x7f, v26
	v_lshrrev_b32_e32 v10, 7, v26
	v_lshlrev_b32_e32 v11, 7, v11
	v_lshl_or_b32 v10, v10, 18, v11
	v_mov_b32_e32 v11, 0
	v_and_b32_e32 v27, 0x7f, v32
	v_lshrrev_b32_e32 v26, 7, v32
	v_lshlrev_b32_e32 v27, 7, v27
	v_lshl_or_b32 v26, v26, 18, v27
	v_mov_b32_e32 v27, 0
	v_lshl_add_u64 v[48:49], v[16:17], 0, v[8:9]
	v_lshl_add_u64 v[50:51], v[16:17], 0, v[10:11]
	v_lshl_add_u64 v[52:53], v[16:17], 0, v[26:27]
	global_load_dwordx2 v[54:55], v[48:49], off
	global_load_dwordx2 v[34:35], v[50:51], off
	global_load_dwordx2 v[32:33], v[52:53], off
	global_load_dwordx4 v[8:11], v[30:31], off offset:16
	global_load_dwordx4 v[40:43], v[18:19], off offset:1024
	v_lshl_add_u64 v[100:101], v[44:45], 0, s[24:25]
	global_load_dwordx2 v[60:61], v[100:101], off
	v_lshl_add_u64 v[102:103], v[44:45], 0, s[26:27]
	global_load_dwordx2 v[62:63], v[102:103], off
	v_lshl_add_u64 v[100:101], v[44:45], 0, s[28:29]
	global_load_dwordx2 v[64:65], v[100:101], off
	v_lshl_add_u64 v[102:103], v[48:49], 0, s[24:25]
	global_load_dwordx2 v[66:67], v[102:103], off
	v_lshl_add_u64 v[100:101], v[48:49], 0, s[26:27]
	global_load_dwordx2 v[68:69], v[100:101], off
	v_lshl_add_u64 v[102:103], v[48:49], 0, s[28:29]
	global_load_dwordx2 v[70:71], v[102:103], off
	v_lshl_add_u64 v[100:101], v[50:51], 0, s[24:25]
	global_load_dwordx2 v[72:73], v[100:101], off
	v_lshl_add_u64 v[102:103], v[50:51], 0, s[26:27]
	global_load_dwordx2 v[74:75], v[102:103], off
	v_lshl_add_u64 v[100:101], v[50:51], 0, s[28:29]
	global_load_dwordx2 v[76:77], v[100:101], off
	v_lshl_add_u64 v[102:103], v[52:53], 0, s[24:25]
	global_load_dwordx2 v[78:79], v[102:103], off
	v_lshl_add_u64 v[100:101], v[52:53], 0, s[26:27]
	global_load_dwordx2 v[80:81], v[100:101], off
	v_lshl_add_u64 v[102:103], v[52:53], 0, s[28:29]
	global_load_dwordx2 v[82:83], v[102:103], off
	v_mov_b32_e32 v26, v3
	s_waitcnt vmcnt(19)
	v_lshlrev_b32_e32 v56, 16, v36
	v_and_b32_e32 v57, 0xffff0000, v36
	v_lshlrev_b32_e32 v36, 16, v37
	v_and_b32_e32 v37, 0xffff0000, v37
	v_lshlrev_b32_e32 v58, 16, v38
	v_and_b32_e32 v59, 0xffff0000, v38
	v_lshlrev_b32_e32 v38, 16, v39
	v_and_b32_e32 v39, 0xffff0000, v39
	s_waitcnt vmcnt(17)
	v_cvt_pk_f32_fp8_e32 v[44:45], v46
	v_cvt_pk_f32_fp8_sdwa v[48:49], v46 src0_sel:WORD_1
	v_cvt_pk_f32_fp8_e32 v[50:51], v47
	v_cvt_pk_f32_fp8_sdwa v[46:47], v47 src0_sel:WORD_1
	v_pk_fma_f32 v[44:45], v[0:1], v[44:45], 0 op_sel_hi:[0,1,0]
	v_pk_fma_f32 v[48:49], v[0:1], v[48:49], 0 op_sel_hi:[0,1,0]
	v_pk_fma_f32 v[50:51], v[0:1], v[50:51], 0 op_sel_hi:[0,1,0]
	v_pk_fma_f32 v[46:47], v[0:1], v[46:47], 0 op_sel_hi:[0,1,0]
	s_waitcnt vmcnt(16)
	v_cvt_pk_f32_fp8_e32 v[52:53], v54
	v_cvt_pk_f32_fp8_sdwa v[84:85], v54 src0_sel:WORD_1
	v_cvt_pk_f32_fp8_e32 v[86:87], v55
	v_cvt_pk_f32_fp8_sdwa v[54:55], v55 src0_sel:WORD_1
	s_waitcnt vmcnt(15)
	v_cvt_pk_f32_fp8_e32 v[88:89], v34
	v_cvt_pk_f32_fp8_sdwa v[90:91], v34 src0_sel:WORD_1
	v_cvt_pk_f32_fp8_e32 v[92:93], v35
	v_cvt_pk_f32_fp8_sdwa v[34:35], v35 src0_sel:WORD_1
	s_waitcnt vmcnt(14)
	v_cvt_pk_f32_fp8_e32 v[94:95], v32
	v_cvt_pk_f32_fp8_sdwa v[96:97], v32 src0_sel:WORD_1
	v_cvt_pk_f32_fp8_e32 v[98:99], v33
	v_cvt_pk_f32_fp8_sdwa v[32:33], v33 src0_sel:WORD_1
	v_pk_fma_f32 v[44:45], v[0:1], v[52:53], v[44:45] op_sel:[1,0,0]
	v_pk_fma_f32 v[48:49], v[0:1], v[84:85], v[48:49] op_sel:[1,0,0]
	v_pk_fma_f32 v[50:51], v[0:1], v[86:87], v[50:51] op_sel:[1,0,0]
	v_pk_fma_f32 v[46:47], v[0:1], v[54:55], v[46:47] op_sel:[1,0,0]
	v_pk_fma_f32 v[48:49], v[2:3], v[90:91], v[48:49] op_sel_hi:[0,1,1]
	v_pk_fma_f32 v[44:45], v[2:3], v[88:89], v[44:45] op_sel_hi:[0,1,1]
	v_pk_fma_f32 v[34:35], v[2:3], v[34:35], v[46:47] op_sel_hi:[0,1,1]
	v_pk_fma_f32 v[46:47], v[2:3], v[92:93], v[50:51] op_sel_hi:[0,1,1]
	v_pk_fma_f32 v[44:45], v[26:27], v[94:95], v[44:45] op_sel_hi:[0,1,1]
	v_pk_fma_f32 v[48:49], v[26:27], v[96:97], v[48:49] op_sel_hi:[0,1,1]
	v_pk_fma_f32 v[46:47], v[26:27], v[98:99], v[46:47] op_sel_hi:[0,1,1]
	v_pk_fma_f32 v[32:33], v[26:27], v[32:33], v[34:35] op_sel_hi:[0,1,1]
	v_pk_fma_f32 v[6:7], v[48:49], v[6:7], v[36:37]
	v_pk_fma_f32 v[4:5], v[44:45], v[4:5], v[56:57]
	s_waitcnt vmcnt(13)
	v_pk_fma_f32 v[10:11], v[32:33], v[10:11], v[38:39]
	v_pk_fma_f32 v[8:9], v[46:47], v[8:9], v[58:59]
	global_store_dwordx4 v[22:23], v[4:7], off offset:-4096
	global_store_dwordx4 v[22:23], v[8:11], off offset:-4080
	global_load_dwordx4 v[4:7], v[30:31], off offset:2048
	s_nop 0
	global_load_dwordx4 v[8:11], v[30:31], off offset:2064
	global_load_dwordx4 v[32:35], v[18:19], off offset:2048
	s_waitcnt vmcnt(16)
	v_cvt_pk_f32_fp8_e32 v[44:45], v60
	v_cvt_pk_f32_fp8_sdwa v[46:47], v60 src0_sel:WORD_1
	v_cvt_pk_f32_fp8_e32 v[48:49], v61
	v_cvt_pk_f32_fp8_sdwa v[50:51], v61 src0_sel:WORD_1
	s_waitcnt vmcnt(13)
	v_cvt_pk_f32_fp8_e32 v[52:53], v66
	v_cvt_pk_f32_fp8_sdwa v[54:55], v66 src0_sel:WORD_1
	v_cvt_pk_f32_fp8_e32 v[56:57], v67
	v_cvt_pk_f32_fp8_sdwa v[58:59], v67 src0_sel:WORD_1
	s_waitcnt vmcnt(10)
	v_cvt_pk_f32_fp8_e32 v[60:61], v72
	v_cvt_pk_f32_fp8_sdwa v[66:67], v72 src0_sel:WORD_1
	v_cvt_pk_f32_fp8_e32 v[84:85], v73
	v_cvt_pk_f32_fp8_sdwa v[72:73], v73 src0_sel:WORD_1
	s_waitcnt vmcnt(7)
	v_cvt_pk_f32_fp8_e32 v[86:87], v78
	v_cvt_pk_f32_fp8_sdwa v[88:89], v78 src0_sel:WORD_1
	v_cvt_pk_f32_fp8_e32 v[90:91], v79
	v_cvt_pk_f32_fp8_sdwa v[78:79], v79 src0_sel:WORD_1
	v_pk_fma_f32 v[46:47], v[0:1], v[46:47], 0 op_sel_hi:[0,1,0]
	v_pk_fma_f32 v[44:45], v[0:1], v[44:45], 0 op_sel_hi:[0,1,0]
	v_pk_fma_f32 v[50:51], v[0:1], v[50:51], 0 op_sel_hi:[0,1,0]
	v_pk_fma_f32 v[48:49], v[0:1], v[48:49], 0 op_sel_hi:[0,1,0]
	v_pk_fma_f32 v[44:45], v[0:1], v[52:53], v[44:45] op_sel:[1,0,0]
	v_pk_fma_f32 v[46:47], v[0:1], v[54:55], v[46:47] op_sel:[1,0,0]
	v_pk_fma_f32 v[48:49], v[0:1], v[56:57], v[48:49] op_sel:[1,0,0]
	v_pk_fma_f32 v[50:51], v[0:1], v[58:59], v[50:51] op_sel:[1,0,0]
	v_pk_fma_f32 v[46:47], v[2:3], v[66:67], v[46:47] op_sel_hi:[0,1,1]
	v_pk_fma_f32 v[44:45], v[2:3], v[60:61], v[44:45] op_sel_hi:[0,1,1]
	v_lshlrev_b32_e32 v36, 16, v40
	v_and_b32_e32 v37, 0xffff0000, v40
	v_lshlrev_b32_e32 v38, 16, v41
	v_and_b32_e32 v39, 0xffff0000, v41
	v_pk_fma_f32 v[50:51], v[2:3], v[72:73], v[50:51] op_sel_hi:[0,1,1]
	v_pk_fma_f32 v[48:49], v[2:3], v[84:85], v[48:49] op_sel_hi:[0,1,1]
	v_pk_fma_f32 v[44:45], v[26:27], v[86:87], v[44:45] op_sel_hi:[0,1,1]
	v_pk_fma_f32 v[46:47], v[26:27], v[88:89], v[46:47] op_sel_hi:[0,1,1]
	v_lshlrev_b32_e32 v40, 16, v42
	v_and_b32_e32 v41, 0xffff0000, v42
	v_lshlrev_b32_e32 v42, 16, v43
	v_and_b32_e32 v43, 0xffff0000, v43
	v_pk_fma_f32 v[48:49], v[26:27], v[90:91], v[48:49] op_sel_hi:[0,1,1]
	v_pk_fma_f32 v[50:51], v[26:27], v[78:79], v[50:51] op_sel_hi:[0,1,1]
	v_lshl_add_u64 v[30:31], v[28:29], 0, s[16:17]
	v_cvt_pk_f32_fp8_sdwa v[52:53], v68 src0_sel:WORD_1
	v_cvt_pk_f32_fp8_e32 v[54:55], v69
	v_cvt_pk_f32_fp8_sdwa v[56:57], v69 src0_sel:WORD_1
	v_cvt_pk_f32_fp8_e32 v[58:59], v74
	v_cvt_pk_f32_fp8_sdwa v[60:61], v74 src0_sel:WORD_1
	v_cvt_pk_f32_fp8_sdwa v[66:67], v75 src0_sel:WORD_1
	s_waitcnt vmcnt(6)
	v_cvt_pk_f32_fp8_sdwa v[72:73], v80 src0_sel:WORD_1
	v_cvt_pk_f32_fp8_sdwa v[78:79], v81 src0_sel:WORD_1
	v_lshl_add_u64 v[28:29], v[28:29], 0, s[18:19]
	s_waitcnt vmcnt(2)
	v_pk_fma_f32 v[6:7], v[46:47], v[6:7], v[38:39]
	v_pk_fma_f32 v[4:5], v[44:45], v[4:5], v[36:37]
	s_waitcnt vmcnt(1)
	v_pk_fma_f32 v[10:11], v[50:51], v[10:11], v[42:43]
	v_pk_fma_f32 v[8:9], v[48:49], v[8:9], v[40:41]
	global_store_dwordx4 v[22:23], v[4:7], off offset:-2048
	global_store_dwordx4 v[22:23], v[8:11], off offset:-2032
	global_load_dwordx4 v[4:7], v[24:25], off
	s_nop 0
	global_load_dwordx4 v[8:11], v[30:31], off offset:16
	global_load_dwordx4 v[36:39], v[18:19], off offset:3072
	v_cvt_pk_f32_fp8_e32 v[42:43], v62
	v_cvt_pk_f32_fp8_sdwa v[44:45], v62 src0_sel:WORD_1
	v_cvt_pk_f32_fp8_e32 v[46:47], v63
	v_cvt_pk_f32_fp8_sdwa v[48:49], v63 src0_sel:WORD_1
	v_cvt_pk_f32_fp8_e32 v[50:51], v68
	v_cvt_pk_f32_fp8_e32 v[62:63], v75
	v_cvt_pk_f32_fp8_e32 v[68:69], v80
	v_cvt_pk_f32_fp8_e32 v[74:75], v81
	v_pk_fma_f32 v[44:45], v[0:1], v[44:45], 0 op_sel_hi:[0,1,0]
	v_pk_fma_f32 v[42:43], v[0:1], v[42:43], 0 op_sel_hi:[0,1,0]
	v_pk_fma_f32 v[48:49], v[0:1], v[48:49], 0 op_sel_hi:[0,1,0]
	v_pk_fma_f32 v[46:47], v[0:1], v[46:47], 0 op_sel_hi:[0,1,0]
	v_pk_fma_f32 v[42:43], v[0:1], v[50:51], v[42:43] op_sel:[1,0,0]
	v_pk_fma_f32 v[44:45], v[0:1], v[52:53], v[44:45] op_sel:[1,0,0]
	v_pk_fma_f32 v[46:47], v[0:1], v[54:55], v[46:47] op_sel:[1,0,0]
	v_pk_fma_f32 v[48:49], v[0:1], v[56:57], v[48:49] op_sel:[1,0,0]
	v_pk_fma_f32 v[44:45], v[2:3], v[60:61], v[44:45] op_sel_hi:[0,1,1]
	v_pk_fma_f32 v[42:43], v[2:3], v[58:59], v[42:43] op_sel_hi:[0,1,1]
	s_waitcnt vmcnt(5)
	v_lshlrev_b32_e32 v30, 16, v32
	v_and_b32_e32 v31, 0xffff0000, v32
	v_lshlrev_b32_e32 v32, 16, v33
	v_and_b32_e32 v33, 0xffff0000, v33
	v_pk_fma_f32 v[48:49], v[2:3], v[66:67], v[48:49] op_sel_hi:[0,1,1]
	v_pk_fma_f32 v[46:47], v[2:3], v[62:63], v[46:47] op_sel_hi:[0,1,1]
	v_pk_fma_f32 v[42:43], v[26:27], v[68:69], v[42:43] op_sel_hi:[0,1,1]
	v_pk_fma_f32 v[44:45], v[26:27], v[72:73], v[44:45] op_sel_hi:[0,1,1]
	v_lshlrev_b32_e32 v40, 16, v34
	v_and_b32_e32 v41, 0xffff0000, v34
	v_lshlrev_b32_e32 v34, 16, v35
	v_and_b32_e32 v35, 0xffff0000, v35
	v_pk_fma_f32 v[46:47], v[26:27], v[74:75], v[46:47] op_sel_hi:[0,1,1]
	v_pk_fma_f32 v[48:49], v[26:27], v[78:79], v[48:49] op_sel_hi:[0,1,1]
	v_cvt_pk_f32_fp8_e32 v[50:51], v76
	v_cvt_pk_f32_fp8_sdwa v[52:53], v76 src0_sel:WORD_1
	v_cvt_pk_f32_fp8_e32 v[54:55], v77
	v_cvt_pk_f32_fp8_sdwa v[56:57], v77 src0_sel:WORD_1
	v_cvt_pk_f32_fp8_e32 v[58:59], v82
	v_cvt_pk_f32_fp8_sdwa v[60:61], v82 src0_sel:WORD_1
	v_cvt_pk_f32_fp8_e32 v[62:63], v83
	v_lshl_add_u64 v[18:19], v[18:19], 0, s[8:9]
	s_waitcnt vmcnt(2)
	v_pk_fma_f32 v[6:7], v[44:45], v[6:7], v[32:33]
	v_pk_fma_f32 v[4:5], v[42:43], v[4:5], v[30:31]
	s_waitcnt vmcnt(1)
	v_pk_fma_f32 v[10:11], v[48:49], v[10:11], v[34:35]
	v_pk_fma_f32 v[8:9], v[46:47], v[8:9], v[40:41]
	global_store_dwordx4 v[22:23], v[4:7], off
	global_store_dwordx4 v[22:23], v[8:11], off offset:16
	global_load_dwordx4 v[4:7], v[24:25], off offset:2048
	s_nop 0
	global_load_dwordx4 v[8:11], v[28:29], off offset:16
	s_waitcnt vmcnt(4)
	v_lshlrev_b32_e32 v24, 16, v36
	v_and_b32_e32 v25, 0xffff0000, v36
	v_lshlrev_b32_e32 v28, 16, v37
	v_and_b32_e32 v29, 0xffff0000, v37
	v_cvt_pk_f32_fp8_e32 v[34:35], v64
	v_cvt_pk_f32_fp8_sdwa v[36:37], v64 src0_sel:WORD_1
	v_lshlrev_b32_e32 v30, 16, v38
	v_and_b32_e32 v31, 0xffff0000, v38
	v_lshlrev_b32_e32 v32, 16, v39
	v_and_b32_e32 v33, 0xffff0000, v39
	v_cvt_pk_f32_fp8_e32 v[38:39], v65
	v_cvt_pk_f32_fp8_sdwa v[40:41], v65 src0_sel:WORD_1
	v_cvt_pk_f32_fp8_e32 v[42:43], v70
	v_cvt_pk_f32_fp8_sdwa v[44:45], v70 src0_sel:WORD_1
	v_cvt_pk_f32_fp8_e32 v[46:47], v71
	v_cvt_pk_f32_fp8_sdwa v[48:49], v71 src0_sel:WORD_1
	v_cvt_pk_f32_fp8_sdwa v[64:65], v83 src0_sel:WORD_1
	v_pk_fma_f32 v[36:37], v[0:1], v[36:37], 0 op_sel_hi:[0,1,0]
	v_pk_fma_f32 v[34:35], v[0:1], v[34:35], 0 op_sel_hi:[0,1,0]
	v_pk_fma_f32 v[40:41], v[0:1], v[40:41], 0 op_sel_hi:[0,1,0]
	v_pk_fma_f32 v[38:39], v[0:1], v[38:39], 0 op_sel_hi:[0,1,0]
	v_pk_fma_f32 v[34:35], v[0:1], v[42:43], v[34:35] op_sel:[1,0,0]
	v_pk_fma_f32 v[36:37], v[0:1], v[44:45], v[36:37] op_sel:[1,0,0]
	v_pk_fma_f32 v[38:39], v[0:1], v[46:47], v[38:39] op_sel:[1,0,0]
	v_pk_fma_f32 v[0:1], v[0:1], v[48:49], v[40:41] op_sel:[1,0,0]
	v_pk_fma_f32 v[36:37], v[2:3], v[52:53], v[36:37] op_sel_hi:[0,1,1]
	v_pk_fma_f32 v[34:35], v[2:3], v[50:51], v[34:35] op_sel_hi:[0,1,1]
	v_pk_fma_f32 v[0:1], v[2:3], v[56:57], v[0:1] op_sel_hi:[0,1,1]
	v_pk_fma_f32 v[2:3], v[2:3], v[54:55], v[38:39] op_sel_hi:[0,1,1]
	v_pk_fma_f32 v[34:35], v[26:27], v[58:59], v[34:35] op_sel_hi:[0,1,1]
	v_pk_fma_f32 v[36:37], v[26:27], v[60:61], v[36:37] op_sel_hi:[0,1,1]
	v_pk_fma_f32 v[38:39], v[26:27], v[62:63], v[2:3] op_sel_hi:[0,1,1]
	v_pk_fma_f32 v[26:27], v[26:27], v[64:65], v[0:1] op_sel_hi:[0,1,1]
	s_waitcnt vmcnt(1)
	v_pk_fma_f32 v[2:3], v[36:37], v[6:7], v[28:29]
	v_pk_fma_f32 v[0:1], v[34:35], v[4:5], v[24:25]
	s_waitcnt vmcnt(0)
	v_pk_fma_f32 v[6:7], v[26:27], v[10:11], v[32:33]
	v_pk_fma_f32 v[4:5], v[38:39], v[8:9], v[30:31]
	global_store_dwordx4 v[22:23], v[0:3], off offset:2048
	global_store_dwordx4 v[22:23], v[4:7], off offset:2064
	v_lshl_add_u64 v[22:23], v[22:23], 0, s[10:11]
	s_andn2_b64 exec, exec, s[12:13]
	s_cbranch_execnz .LBB0_1094
